# b1/noise LDS reads moved ahead of the reduce barrier, denser relu/cvt interleave in the last k-step, branch-free out-tile write
# speedup vs baseline: 1.0055x; 1.0055x over previous
.LBB1_2:
	v_lshrrev_b32_e32 v151, 4, v137
	s_lshl_b64 s[6:7], s[2:3], 4
	v_cmp_eq_u32_e64 s[2:3], 1, v151
	s_waitcnt vmcnt(31)
	v_cvt_f16_f32_e32 v8, v8
	v_cmp_gt_u32_e32 vcc, 16, v137
	s_waitcnt vmcnt(29)
	v_cndmask_b32_e64 v116, 0, v116, s[2:3]
	s_waitcnt vmcnt(21)
	v_cndmask_b32_e64 v100, 0, v100, s[2:3]
	v_cmp_eq_u32_e64 s[0:1], 2, v151
	v_cndmask_b32_e64 v114, 0, v114, s[2:3]
	v_cndmask_b32_e64 v115, 0, v115, s[2:3]
	v_cndmask_b32_e32 v6, v116, v6, vcc
	v_cndmask_b32_e64 v116, 0, v117, s[2:3]
	v_cndmask_b32_e64 v108, 0, v108, s[2:3]
	v_cndmask_b32_e32 v26, v100, v26, vcc
	v_cvt_f16_f32_e32 v29, v29
	v_cndmask_b32_e64 v100, 0, v101, s[2:3]
	v_cndmask_b32_e32 v28, 0, v28, vcc
	v_cndmask_b32_e64 v152, 0, 1.0, s[0:1]
	v_cndmask_b32_e32 v114, v114, v120, vcc
	v_cndmask_b32_e32 v115, v115, v121, vcc
	v_cndmask_b32_e32 v7, v116, v7, vcc
	v_cndmask_b32_e64 v106, 0, v106, s[2:3]
	v_cndmask_b32_e64 v107, 0, v107, s[2:3]
	v_cndmask_b32_e32 v14, v108, v14, vcc
	v_cndmask_b32_e64 v108, 0, v109, s[2:3]
	v_cndmask_b32_e32 v27, v100, v27, vcc
	v_cvt_f16_f32_e32 v100, v28
	v_cndmask_b32_e32 v116, 0, v8, vcc
	v_cvt_pk_f16_f32 v8, v6, v7
	v_cvt_pk_f16_f32 v7, v114, v115
	v_cndmask_b32_e64 v114, v152, v140, s[2:3]
	v_cndmask_b32_e32 v106, v106, v112, vcc
	v_cndmask_b32_e32 v107, v107, v113, vcc
	v_cndmask_b32_e32 v15, v108, v15, vcc
	v_cndmask_b32_e64 v98, 0, v98, s[2:3]
	v_cndmask_b32_e64 v99, 0, v99, s[2:3]
	v_cndmask_b32_e32 v110, v114, v110, vcc
	v_cndmask_b32_e64 v114, 0, v141, s[2:3]
	v_cndmask_b32_e32 v108, 0, v16, vcc
	v_cvt_pk_f16_f32 v16, v14, v15
	v_cvt_pk_f16_f32 v15, v106, v107
	v_cndmask_b32_e64 v106, v152, v138, s[2:3]
	v_cndmask_b32_e32 v98, v98, v104, vcc
	v_cndmask_b32_e32 v99, v99, v105, vcc
	v_cndmask_b32_e32 v111, v114, v111, vcc
	v_cndmask_b32_e32 v102, v106, v102, vcc
	v_cndmask_b32_e64 v106, 0, v139, s[2:3]
	v_cndmask_b32_e32 v29, 0, v29, vcc
	v_cvt_pk_f16_f32 v28, v26, v27
	v_cvt_pk_f16_f32 v27, v98, v99
	v_lshlrev_b32_e32 v101, 10, v1
	v_bitop3_b32 v98, v151, v0, 3 bitop3:0x78
	v_lshl_add_u64 v[130:131], s[4:5], 0, v[130:131]
	v_cvt_f16_f32_e32 v4, v4
	v_cvt_pk_f16_f32 v14, v110, v111
	v_cndmask_b32_e32 v103, v106, v103, vcc
	v_pack_b32_f16 v29, v100, v29
	v_lshl_or_b32 v111, v98, 4, v101
	v_lshlrev_b32_e32 v100, 4, v1
	s_movk_i32 s4, 0xc0
	v_cndmask_b32_e64 v124, 0, v124, s[2:3]
	v_cvt_pk_f16_f32 v26, v102, v103
	v_and_b32_e32 v112, 0xc0, v100
	v_bitop3_b32 v100, v100, s4, v111 bitop3:0x26
	s_lshl_b32 s4, s20, 3
	v_lshrrev_b32_e32 v102, 5, v137
	v_lshrrev_b32_e32 v104, 1, v137
	v_cndmask_b32_e64 v122, 0, v122, s[2:3]
	v_cndmask_b32_e64 v123, 0, v123, s[2:3]
	v_cndmask_b32_e32 v2, v124, v2, vcc
	v_cvt_f16_f32_e32 v5, v5
	v_cndmask_b32_e64 v124, 0, v125, s[2:3]
	v_cvt_f16_f32_e32 v9, v9
	v_or_b32_e32 v103, s4, v102
	v_and_or_b32 v110, v104, 8, v101
	v_bitop3_b32 v101, s4, v1, v102 bitop3:0x36
	s_lshl_b32 s4, s20, 4
	v_cndmask_b32_e32 v122, v122, v128, vcc
	v_cndmask_b32_e32 v123, v123, v129, vcc
	v_cndmask_b32_e32 v3, v124, v3, vcc
	v_cndmask_b32_e32 v17, 0, v17, vcc
	v_lshlrev_b32_e32 v107, 4, v101
	v_bitop3_b32 v101, v103, v1, 2 bitop3:0x36
	s_add_i32 s4, s4, 0x10000
	v_bfe_u32 v0, v0, 4, 2
	v_cndmask_b32_e64 v144, v152, v144, s[2:3]
	v_cndmask_b32_e32 v124, 0, v4, vcc
	v_cvt_pk_f16_f32 v4, v2, v3
	v_cvt_pk_f16_f32 v3, v122, v123
	v_cndmask_b32_e64 v122, v152, v142, s[2:3]
	v_cvt_pk_f16_f32 v17, v108, v17
	s_movk_i32 s5, 0x80
	v_lshlrev_b32_e32 v108, 4, v101
	v_bitop3_b32 v101, v103, v1, 4 bitop3:0x36
	s_cmp_lt_u32 s22, 64
	v_lshlrev_b32_e32 v104, 5, v0
	v_lshlrev_b32_e32 v0, 6, v0
	v_cndmask_b32_e32 v126, v144, v126, vcc
	v_cndmask_b32_e64 v144, 0, v145, s[2:3]
	v_cndmask_b32_e32 v118, v122, v118, vcc
	v_cndmask_b32_e64 v122, 0, v143, s[2:3]
	v_bitop3_b32 v99, v112, s5, v111 bitop3:0x36
	v_lshlrev_b32_e32 v109, 4, v101
	v_bitop3_b32 v101, v103, v1, 6 bitop3:0x36
	v_lshl_or_b32 v105, s20, 8, v0
	v_mov_b32_e32 v0, 0x1ec00
	s_cselect_b64 s[4:5], -1, 0
	v_cndmask_b32_e32 v127, v144, v127, vcc
	v_cndmask_b32_e32 v5, 0, v5, vcc
	v_cndmask_b32_e32 v119, v122, v119, vcc
	v_cndmask_b32_e32 v9, 0, v9, vcc
	v_lshlrev_b32_e32 v113, 4, v101
	v_lshlrev_b32_e32 v101, 5, v1
	v_lshl_add_u32 v106, v137, 6, v0
	s_cmp_eq_u32 s20, 0
	s_cselect_b32 s31, 0, 0xffff1d00
	v_add_u32_e32 v106, s31, v106
	v_cndmask_b32_e64 v0, 0, 1, s[4:5]
	v_lshl_add_u64 v[132:133], s[8:9], 0, v[132:133]
	v_or_b32_e32 v148, 0x400, v147
	v_or_b32_e32 v149, 0x800, v147
	v_or_b32_e32 v150, 0xc00, v147
	v_cvt_pk_f16_f32 v2, v126, v127
	v_pack_b32_f16 v5, v124, v5
	v_cvt_pk_f16_f32 v6, v118, v119
	v_pack_b32_f16 v9, v116, v9
	v_bitop3_b32 v98, v112, 64, v111 bitop3:0x36
	v_lshl_or_b32 v104, s20, 7, v104
	s_mov_b32 s22, 0x98000
	s_mov_b32 s23, 0x5040100
	s_mov_b32 s24, 0x7060302
	v_add_u32_e32 v107, v107, v110
	v_add_u32_e32 v108, v108, v110
	v_add_u32_e32 v109, v109, v110
	v_add_u32_e32 v110, v113, v110
	v_add_u32_e32 v111, v112, v111
	v_lshlrev_b32_e32 v113, 4, v137
	v_or_b32_e32 v113, 0x10000, v113
	s_lshr_b32 s28, s20, 2
	s_and_b32 s29, s20, 3
	s_lshl_b32 s28, s28, 10
	s_lshl_b32 s29, s29, 2
	s_add_i32 s28, s28, s29
	v_add_u32_e32 v112, s28, v113
	v_cmp_eq_u32_e64 s[26:27], 3, v151
	v_add_u32_e32 v114, 0x12400, v101
	v_cmp_ne_u32_e64 s[4:5], 1, v0
	s_waitcnt vmcnt(16)
	v_cndmask_b32_e64 v1, v30, v134, s[0:1]
	v_bfi_b32 v30, s10, v1, v30
	v_perm_b32 v1, v22, v134, s24
	v_cndmask_b32_e64 v22, v22, v1, s[0:1]
	v_bfi_b32 v1, s10, v135, v18
	v_perm_b32 v121, v10, v135, s24
	v_cndmask_b32_e64 v18, v18, v1, s[0:1]
	v_cndmask_b32_e64 v10, v10, v121, s[0:1]
	v_mov_b32_e32 v121, v136
	v_mov_b32_e32 v144, v136
	v_mov_b32_e32 v145, v136
	v_mov_b32_e32 v0, v136
	v_mov_b32_e32 v1, v136
	s_waitcnt lgkmcnt(0)
	s_barrier
	ds_read_u16 v102, v114
	ds_read_u16 v103, v114 offset:512
	ds_read_u16 v115, v114 offset:1024
	ds_read_u16 v116, v114 offset:1536
	v_add_u32_e32 v0, 0x12c00, v105
	ds_read_b128 v[240:243], v0
	ds_read_b128 v[244:247], v0 offset:16
	ds_read_b128 v[248:251], v0 offset:32
	ds_read_b128 v[252:255], v0 offset:48
	v_add_u32_e32 v114, 2, v114
	s_branch .LBB1_4

.LBB1_4:
	s_waitcnt lgkmcnt(0)
	s_and_saveexec_b64 s[8:9], s[2:3]
	v_perm_b32 v5, v1, v102, s23
	v_perm_b32 v9, v121, v103, s23
	v_perm_b32 v17, v144, v115, s23
	v_perm_b32 v29, v145, v116, s23
	s_or_b64 exec, exec, s[8:9]
	v_mfma_f32_16x16x32_f16 v[126:129], v[30:33], v[6:9], 0
	s_cmp_lg_u32 s22, 0x818000
	v_mfma_f32_16x16x32_f16 v[122:125], v[30:33], v[2:5], 0
	s_cselect_b32 s9, s11, 15
	s_nop 2
	v_cvt_pk_f16_f32 v121, v126, v127
	v_cvt_pk_f16_f32 v127, v128, v129
	v_mfma_f32_16x16x32_f16 v[134:137], v[30:33], v[14:17], 0
	v_pk_max_f16 v126, v121, 0
	s_nop 0
	v_cvt_pk_f16_f32 v0, v122, v123
	v_cvt_pk_f16_f32 v1, v124, v125
	v_mfma_f32_16x16x32_f16 v[30:33], v[30:33], v[26:29], 0
	v_pk_max_f16 v127, v127, 0
	v_pk_max_f16 v0, v0, 0
	v_pk_max_f16 v1, v1, 0
	v_mfma_f32_16x16x32_f16 v[122:125], v[22:25], v[2:5], 0
	ds_write2st64_b64 v107, v[0:1], v[126:127] offset1:32
	s_nop 1
	v_cvt_pk_f16_f32 v0, v134, v135
	v_cvt_pk_f16_f32 v1, v136, v137
	v_mfma_f32_16x16x32_f16 v[126:129], v[22:25], v[6:9], 0
	s_nop 0
	v_cvt_pk_f16_f32 v30, v30, v31
	v_cvt_pk_f16_f32 v31, v32, v33
	v_pk_max_f16 v0, v0, 0
	v_mfma_f32_16x16x32_f16 v[134:137], v[22:25], v[14:17], 0
	v_pk_max_f16 v30, v30, 0
	v_pk_max_f16 v31, v31, 0
	v_pk_max_f16 v1, v1, 0
	v_mfma_f32_16x16x32_f16 v[22:25], v[22:25], v[26:29], 0
	ds_write2st64_b64 v107, v[0:1], v[30:31] offset0:64 offset1:96
	v_cvt_pk_f16_f32 v0, v122, v123
	v_cvt_pk_f16_f32 v1, v124, v125
	v_mfma_f32_16x16x32_f16 v[30:33], v[18:21], v[2:5], 0
	v_pk_max_f16 v0, v0, 0
	v_cvt_pk_f16_f32 v139, v128, v129
	v_pk_max_f16 v1, v1, 0
	v_mfma_f32_16x16x32_f16 v[122:125], v[18:21], v[6:9], 0
	v_cvt_pk_f16_f32 v121, v126, v127
	v_pk_max_f16 v138, v121, 0
	v_pk_max_f16 v139, v139, 0
	v_mfma_f32_16x16x32_f16 v[126:129], v[18:21], v[14:17], 0
	ds_write2st64_b64 v108, v[0:1], v[138:139] offset1:32
	v_cvt_pk_f16_f32 v0, v134, v135
	v_cvt_pk_f16_f32 v1, v136, v137
	v_mfma_f32_16x16x32_f16 v[18:21], v[18:21], v[26:29], 0
	v_pk_max_f16 v0, v0, 0
	v_cvt_pk_f16_f32 v139, v24, v25
	v_pk_max_f16 v1, v1, 0
	v_mfma_f32_16x16x32_f16 v[134:137], v[10:13], v[2:5], 0
	v_cvt_pk_f16_f32 v121, v22, v23
	v_pk_max_f16 v138, v121, 0
	v_pk_max_f16 v139, v139, 0
	ds_write2st64_b64 v108, v[0:1], v[138:139] offset0:64 offset1:96
	v_cvt_pk_f16_f32 v0, v30, v31
	v_mfma_f32_16x16x32_f16 v[22:25], v[10:13], v[6:9], 0
	v_cvt_pk_f16_f32 v1, v32, v33
	v_pk_max_f16 v0, v0, 0
	v_cvt_pk_f16_f32 v30, v122, v123
	v_cvt_pk_f16_f32 v31, v124, v125
	v_mfma_f32_16x16x32_f16 v[138:141], v[10:13], v[14:17], 0
	v_pk_max_f16 v1, v1, 0
	v_pk_max_f16 v30, v30, 0
	v_pk_max_f16 v31, v31, 0
	ds_write2st64_b64 v109, v[0:1], v[30:31] offset1:32
	v_cvt_pk_f16_f32 v0, v126, v127
	v_mfma_f32_16x16x32_f16 v[10:13], v[10:13], v[26:29], 0
	v_cvt_pk_f16_f32 v1, v128, v129
	v_pk_max_f16 v0, v0, 0
	v_cvt_pk_f16_f32 v18, v18, v19
	v_cvt_pk_f16_f32 v19, v20, v21
	v_pk_max_f16 v1, v1, 0
	v_pk_max_f16 v18, v18, 0
	v_pk_max_f16 v19, v19, 0
	ds_write2st64_b64 v109, v[0:1], v[18:19] offset0:64 offset1:96
	v_cvt_pk_f16_f32 v0, v134, v135
	v_cvt_pk_f16_f32 v1, v136, v137
	v_pk_max_f16 v0, v0, 0
	v_cvt_pk_f16_f32 v18, v22, v23
	v_cvt_pk_f16_f32 v19, v24, v25
	v_pk_max_f16 v1, v1, 0
	v_pk_max_f16 v18, v18, 0
	v_pk_max_f16 v19, v19, 0
	ds_write2st64_b64 v110, v[0:1], v[18:19] offset1:32
	v_cvt_pk_f16_f32 v0, v138, v139
	v_cvt_pk_f16_f32 v1, v140, v141
	v_pk_max_f16 v0, v0, 0
	v_cvt_pk_f16_f32 v10, v10, v11
	v_cvt_pk_f16_f32 v11, v12, v13
	v_pk_max_f16 v1, v1, 0
	v_pk_max_f16 v10, v10, 0
	v_pk_max_f16 v11, v11, 0
	ds_write2st64_b64 v110, v[0:1], v[10:11] offset0:64 offset1:96
	s_waitcnt lgkmcnt(0)
	s_barrier
	ds_read_b128 v[122:125], v111
	ds_read_b128 v[126:129], v111 offset:16384
	ds_read_b128 v[134:137], v111 offset:32768
	ds_read_b128 v[138:141], v111 offset:49152
	ds_read_b128 v[142:145], v98
	ds_read_b128 v[152:155], v98 offset:16384
	ds_read_b128 v[156:159], v98 offset:32768
	ds_read_b128 v[160:163], v98 offset:49152
	s_lshl_b32 s20, s9, 7
	v_lshl_add_u64 v[0:1], s[20:21], 3, v[132:133]
	s_add_i32 s25, s22, 0xfff88000
	s_lshl_b32 s8, s9, 8
	buffer_load_dwordx4 v[192:195], v147, s[16:19], s25 offen
	buffer_load_dwordx4 v[196:199], v148, s[16:19], s25 offen
	buffer_load_dwordx4 v[200:203], v149, s[16:19], s25 offen
	buffer_load_dwordx4 v[204:207], v150, s[16:19], s25 offen
	s_waitcnt vmcnt(19) lgkmcnt(7)
	v_mfma_f32_16x16x32_f16 v[164:167], v[58:61], v[122:125], v[240:243]
	s_waitcnt lgkmcnt(6)
	v_mfma_f32_16x16x32_f16 v[168:171], v[58:61], v[126:129], v[240:243]
	s_waitcnt lgkmcnt(5)
	v_mfma_f32_16x16x32_f16 v[172:175], v[58:61], v[134:137], v[240:243]
	s_waitcnt lgkmcnt(4)
	v_mfma_f32_16x16x32_f16 v[10:13], v[58:61], v[138:141], v[240:243]
	s_waitcnt vmcnt(18)
	v_mfma_f32_16x16x32_f16 v[58:61], v[54:57], v[122:125], v[244:247]
	v_mfma_f32_16x16x32_f16 v[176:179], v[54:57], v[126:129], v[244:247]
	v_mfma_f32_16x16x32_f16 v[180:183], v[54:57], v[134:137], v[244:247]
	v_mfma_f32_16x16x32_f16 v[18:21], v[54:57], v[138:141], v[244:247]
	s_waitcnt vmcnt(17)
	v_mfma_f32_16x16x32_f16 v[54:57], v[50:53], v[122:125], v[248:251]
	v_mfma_f32_16x16x32_f16 v[184:187], v[50:53], v[126:129], v[248:251]
	v_mfma_f32_16x16x32_f16 v[188:191], v[50:53], v[134:137], v[248:251]
	v_mfma_f32_16x16x32_f16 v[22:25], v[50:53], v[138:141], v[248:251]
	s_waitcnt vmcnt(16)
	v_mfma_f32_16x16x32_f16 v[50:53], v[38:41], v[122:125], v[252:255]
	v_mfma_f32_16x16x32_f16 v[122:125], v[38:41], v[126:129], v[252:255]
	v_mfma_f32_16x16x32_f16 v[126:129], v[38:41], v[134:137], v[252:255]
	v_mfma_f32_16x16x32_f16 v[38:41], v[38:41], v[138:141], v[252:255]
	ds_read_b128 v[136:139], v99
	ds_read_b128 v[208:211], v99 offset:16384
	ds_read_b128 v[212:215], v99 offset:32768
	ds_read_b128 v[216:219], v99 offset:49152
	s_add_i32 s9, s22, 0xfff90000
	s_waitcnt vmcnt(15) lgkmcnt(7)
	v_mfma_f32_16x16x32_f16 v[164:167], v[94:97], v[142:145], v[164:167]
	s_waitcnt lgkmcnt(6)
	v_mfma_f32_16x16x32_f16 v[168:171], v[94:97], v[152:155], v[168:171]
	s_waitcnt vmcnt(14)
	v_mfma_f32_16x16x32_f16 v[58:61], v[90:93], v[142:145], v[58:61]
	v_mfma_f32_16x16x32_f16 v[176:179], v[90:93], v[152:155], v[176:179]
	s_waitcnt vmcnt(13)
	v_mfma_f32_16x16x32_f16 v[54:57], v[78:81], v[142:145], v[54:57]
	v_mfma_f32_16x16x32_f16 v[184:187], v[78:81], v[152:155], v[184:187]
	s_waitcnt vmcnt(12)
	v_mfma_f32_16x16x32_f16 v[50:53], v[34:37], v[142:145], v[50:53]
	buffer_load_dwordx4 v[140:143], v147, s[16:19], s9 offen
	buffer_load_dwordx4 v[220:223], v148, s[16:19], s9 offen
	v_mfma_f32_16x16x32_f16 v[122:125], v[34:37], v[152:155], v[122:125]
	buffer_load_dwordx4 v[152:155], v149, s[16:19], s9 offen
	buffer_load_dwordx4 v[224:227], v150, s[16:19], s9 offen
	s_mov_b32 s9, s21
	s_waitcnt lgkmcnt(5)
	v_mfma_f32_16x16x32_f16 v[172:175], v[94:97], v[156:159], v[172:175]
	s_waitcnt lgkmcnt(4)
	v_mfma_f32_16x16x32_f16 v[94:97], v[94:97], v[160:163], v[10:13]
	s_nop 2
	v_lshl_add_u64 v[10:11], s[8:9], 4, v[130:131]
	v_mfma_f32_16x16x32_f16 v[180:183], v[90:93], v[156:159], v[180:183]
	v_mfma_f32_16x16x32_f16 v[90:93], v[90:93], v[160:163], v[18:21]
	v_mfma_f32_16x16x32_f16 v[188:191], v[78:81], v[156:159], v[188:191]
	v_mfma_f32_16x16x32_f16 v[78:81], v[78:81], v[160:163], v[22:25]
	global_load_dwordx4 v[30:33], v[10:11], off
	s_nop 1
	global_load_dwordx4 v[22:25], v[10:11], off offset:1024
	global_load_dwordx4 v[18:21], v[10:11], off offset:2048
	s_nop 0
	global_load_dwordx4 v[10:13], v[10:11], off offset:3072
	s_nop 0
	global_load_dwordx2 v[134:135], v[0:1], off
	v_mfma_f32_16x16x32_f16 v[126:129], v[34:37], v[156:159], v[126:129]
	v_mfma_f32_16x16x32_f16 v[34:37], v[34:37], v[160:163], v[38:41]
	s_nop 2
	ds_read_b128 v[38:41], v100
	ds_read_b128 v[156:159], v100 offset:16384
	ds_read_b128 v[160:163], v100 offset:32768
	ds_read_b128 v[228:231], v100 offset:49152
	s_add_i32 s8, s22, 0xfff98000
	s_waitcnt vmcnt(20) lgkmcnt(7)
	v_mfma_f32_16x16x32_f16 v[164:167], v[82:85], v[136:139], v[164:167]
	s_waitcnt lgkmcnt(6)
	v_mfma_f32_16x16x32_f16 v[168:171], v[82:85], v[208:211], v[168:171]
	s_waitcnt lgkmcnt(5)
	v_mfma_f32_16x16x32_f16 v[172:175], v[82:85], v[212:215], v[172:175]
	s_waitcnt lgkmcnt(4)
	v_mfma_f32_16x16x32_f16 v[82:85], v[82:85], v[216:219], v[94:97]
	s_waitcnt vmcnt(19)
	v_mfma_f32_16x16x32_f16 v[58:61], v[70:73], v[136:139], v[58:61]
	v_mfma_f32_16x16x32_f16 v[94:97], v[70:73], v[208:211], v[176:179]
	v_mfma_f32_16x16x32_f16 v[176:179], v[70:73], v[212:215], v[180:183]
	v_mfma_f32_16x16x32_f16 v[70:73], v[70:73], v[216:219], v[90:93]
	s_waitcnt vmcnt(18)
	v_mfma_f32_16x16x32_f16 v[54:57], v[62:65], v[136:139], v[54:57]
	v_mfma_f32_16x16x32_f16 v[90:93], v[62:65], v[208:211], v[184:187]
	v_mfma_f32_16x16x32_f16 v[180:183], v[62:65], v[212:215], v[188:191]
	v_mfma_f32_16x16x32_f16 v[62:65], v[62:65], v[216:219], v[78:81]
	s_waitcnt vmcnt(17)
	v_mfma_f32_16x16x32_f16 v[50:53], v[42:45], v[136:139], v[50:53]
	v_mfma_f32_16x16x32_f16 v[78:81], v[42:45], v[208:211], v[122:125]
	v_mfma_f32_16x16x32_f16 v[122:125], v[42:45], v[212:215], v[126:129]
	s_nop 2
	buffer_load_dwordx4 v[126:129], v147, s[16:19], s8 offen
	buffer_load_dwordx4 v[136:139], v148, s[16:19], s8 offen
	buffer_load_dwordx4 v[184:187], v149, s[16:19], s8 offen
	buffer_load_dwordx4 v[188:191], v150, s[16:19], s8 offen
	v_mfma_f32_16x16x32_f16 v[34:37], v[42:45], v[216:219], v[34:37]
	ds_read_b128 v[42:45], v111 offset:256
	ds_read_b128 v[208:211], v111 offset:16640
	ds_read_b128 v[212:215], v111 offset:33024
	ds_read_b128 v[216:219], v111 offset:49408
	s_add_i32 s8, s22, 0xfffa0000
	s_waitcnt vmcnt(20) lgkmcnt(7)
	v_mfma_f32_16x16x32_f16 v[164:167], v[86:89], v[38:41], v[164:167]
	s_waitcnt lgkmcnt(6)
	v_mfma_f32_16x16x32_f16 v[168:171], v[86:89], v[156:159], v[168:171]
	s_waitcnt lgkmcnt(5)
	v_mfma_f32_16x16x32_f16 v[172:175], v[86:89], v[160:163], v[172:175]
	s_waitcnt lgkmcnt(4)
	v_mfma_f32_16x16x32_f16 v[82:85], v[86:89], v[228:231], v[82:85]
	s_waitcnt vmcnt(19)
	v_mfma_f32_16x16x32_f16 v[58:61], v[74:77], v[38:41], v[58:61]
	v_mfma_f32_16x16x32_f16 v[86:89], v[74:77], v[156:159], v[94:97]
	v_mfma_f32_16x16x32_f16 v[94:97], v[74:77], v[160:163], v[176:179]
	v_mfma_f32_16x16x32_f16 v[70:73], v[74:77], v[228:231], v[70:73]
	s_waitcnt vmcnt(18)
	v_mfma_f32_16x16x32_f16 v[54:57], v[66:69], v[38:41], v[54:57]
	v_mfma_f32_16x16x32_f16 v[74:77], v[66:69], v[156:159], v[90:93]
	v_mfma_f32_16x16x32_f16 v[90:93], v[66:69], v[160:163], v[180:183]
	v_mfma_f32_16x16x32_f16 v[62:65], v[66:69], v[228:231], v[62:65]
	s_waitcnt vmcnt(17)
	v_mfma_f32_16x16x32_f16 v[38:41], v[46:49], v[38:41], v[50:53]
	v_mfma_f32_16x16x32_f16 v[50:53], v[46:49], v[156:159], v[78:81]
	v_mfma_f32_16x16x32_f16 v[66:69], v[46:49], v[160:163], v[122:125]
	s_nop 1
	buffer_load_dwordx4 v[78:81], v147, s[16:19], s8 offen
	buffer_load_dwordx4 v[122:125], v148, s[16:19], s8 offen
	buffer_load_dwordx4 v[156:159], v149, s[16:19], s8 offen
	buffer_load_dwordx4 v[160:163], v150, s[16:19], s8 offen
	v_mfma_f32_16x16x32_f16 v[34:37], v[46:49], v[228:231], v[34:37]
	ds_read_b128 v[46:49], v98 offset:256
	ds_read_b128 v[176:179], v98 offset:16640
	ds_read_b128 v[180:183], v98 offset:33024
	ds_read_b128 v[228:231], v98 offset:49408
	s_add_i32 s8, s22, 0xfffa8000
	s_waitcnt vmcnt(20) lgkmcnt(7)
	v_mfma_f32_16x16x32_f16 v[164:167], v[192:195], v[42:45], v[164:167]
	s_waitcnt lgkmcnt(6)
	v_mfma_f32_16x16x32_f16 v[168:171], v[192:195], v[208:211], v[168:171]
	s_waitcnt lgkmcnt(5)
	v_mfma_f32_16x16x32_f16 v[172:175], v[192:195], v[212:215], v[172:175]
	s_waitcnt lgkmcnt(4)
	v_mfma_f32_16x16x32_f16 v[82:85], v[192:195], v[216:219], v[82:85]
	s_waitcnt vmcnt(19)
	v_mfma_f32_16x16x32_f16 v[58:61], v[196:199], v[42:45], v[58:61]
	v_mfma_f32_16x16x32_f16 v[86:89], v[196:199], v[208:211], v[86:89]
	v_mfma_f32_16x16x32_f16 v[94:97], v[196:199], v[212:215], v[94:97]
	v_mfma_f32_16x16x32_f16 v[70:73], v[196:199], v[216:219], v[70:73]
	s_waitcnt vmcnt(18)
	v_mfma_f32_16x16x32_f16 v[54:57], v[200:203], v[42:45], v[54:57]
	v_mfma_f32_16x16x32_f16 v[74:77], v[200:203], v[208:211], v[74:77]
	v_mfma_f32_16x16x32_f16 v[90:93], v[200:203], v[212:215], v[90:93]
	v_mfma_f32_16x16x32_f16 v[62:65], v[200:203], v[216:219], v[62:65]
	s_waitcnt vmcnt(17)
	v_mfma_f32_16x16x32_f16 v[38:41], v[204:207], v[42:45], v[38:41]
	v_mfma_f32_16x16x32_f16 v[42:45], v[204:207], v[208:211], v[50:53]
	v_mfma_f32_16x16x32_f16 v[50:53], v[204:207], v[212:215], v[66:69]
	s_nop 2
	buffer_load_dwordx4 v[66:69], v147, s[16:19], s8 offen
	buffer_load_dwordx4 v[192:195], v148, s[16:19], s8 offen
	buffer_load_dwordx4 v[196:199], v149, s[16:19], s8 offen
	buffer_load_dwordx4 v[200:203], v150, s[16:19], s8 offen
	v_mfma_f32_16x16x32_f16 v[34:37], v[204:207], v[216:219], v[34:37]
	ds_read_b128 v[204:207], v99 offset:256
	ds_read_b128 v[208:211], v99 offset:16640
	ds_read_b128 v[212:215], v99 offset:33024
	ds_read_b128 v[216:219], v99 offset:49408
	s_add_i32 s8, s22, 0xfffb0000
	s_waitcnt vmcnt(20) lgkmcnt(7)
	v_mfma_f32_16x16x32_f16 v[164:167], v[140:143], v[46:49], v[164:167]
	s_waitcnt lgkmcnt(6)
	v_mfma_f32_16x16x32_f16 v[168:171], v[140:143], v[176:179], v[168:171]
	s_waitcnt lgkmcnt(5)
	v_mfma_f32_16x16x32_f16 v[172:175], v[140:143], v[180:183], v[172:175]
	s_waitcnt lgkmcnt(4)
	v_mfma_f32_16x16x32_f16 v[82:85], v[140:143], v[228:231], v[82:85]
	s_waitcnt vmcnt(19)
	v_mfma_f32_16x16x32_f16 v[58:61], v[220:223], v[46:49], v[58:61]
	v_mfma_f32_16x16x32_f16 v[86:89], v[220:223], v[176:179], v[86:89]
	s_waitcnt vmcnt(18)
	v_mfma_f32_16x16x32_f16 v[54:57], v[152:155], v[46:49], v[54:57]
	v_mfma_f32_16x16x32_f16 v[74:77], v[152:155], v[176:179], v[74:77]
	v_mfma_f32_16x16x32_f16 v[90:93], v[152:155], v[180:183], v[90:93]
	v_mfma_f32_16x16x32_f16 v[62:65], v[152:155], v[228:231], v[62:65]
	s_waitcnt vmcnt(17)
	v_mfma_f32_16x16x32_f16 v[38:41], v[224:227], v[46:49], v[38:41]
	v_mfma_f32_16x16x32_f16 v[42:45], v[224:227], v[176:179], v[42:45]
	v_mfma_f32_16x16x32_f16 v[46:49], v[224:227], v[180:183], v[50:53]
	s_nop 2
	buffer_load_dwordx4 v[50:53], v147, s[16:19], s8 offen
	buffer_load_dwordx4 v[140:143], v148, s[16:19], s8 offen
	buffer_load_dwordx4 v[152:155], v149, s[16:19], s8 offen
	buffer_load_dwordx4 v[176:179], v150, s[16:19], s8 offen
	v_mfma_f32_16x16x32_f16 v[94:97], v[220:223], v[180:183], v[94:97]
	v_mfma_f32_16x16x32_f16 v[70:73], v[220:223], v[228:231], v[70:73]
	v_mfma_f32_16x16x32_f16 v[34:37], v[224:227], v[228:231], v[34:37]
	ds_read_b128 v[180:183], v100 offset:256
	ds_read_b128 v[220:223], v100 offset:16640
	ds_read_b128 v[224:227], v100 offset:33024
	ds_read_b128 v[228:231], v100 offset:49408
	s_add_i32 s8, s22, 0xfffb8000
	s_waitcnt vmcnt(15) lgkmcnt(7)
	v_mfma_f32_16x16x32_f16 v[164:167], v[126:129], v[204:207], v[164:167]
	s_waitcnt lgkmcnt(6)
	v_mfma_f32_16x16x32_f16 v[168:171], v[126:129], v[208:211], v[168:171]
	s_waitcnt lgkmcnt(5)
	v_mfma_f32_16x16x32_f16 v[172:175], v[126:129], v[212:215], v[172:175]
	s_waitcnt lgkmcnt(4)
	v_mfma_f32_16x16x32_f16 v[82:85], v[126:129], v[216:219], v[82:85]
	s_waitcnt vmcnt(14)
	v_mfma_f32_16x16x32_f16 v[58:61], v[136:139], v[204:207], v[58:61]
	v_mfma_f32_16x16x32_f16 v[86:89], v[136:139], v[208:211], v[86:89]
	v_mfma_f32_16x16x32_f16 v[94:97], v[136:139], v[212:215], v[94:97]
	v_mfma_f32_16x16x32_f16 v[70:73], v[136:139], v[216:219], v[70:73]
	s_waitcnt vmcnt(13)
	v_mfma_f32_16x16x32_f16 v[54:57], v[184:187], v[204:207], v[54:57]
	v_mfma_f32_16x16x32_f16 v[74:77], v[184:187], v[208:211], v[74:77]
	v_mfma_f32_16x16x32_f16 v[90:93], v[184:187], v[212:215], v[90:93]
	v_mfma_f32_16x16x32_f16 v[62:65], v[184:187], v[216:219], v[62:65]
	s_waitcnt vmcnt(12)
	v_mfma_f32_16x16x32_f16 v[38:41], v[188:191], v[204:207], v[38:41]
	buffer_load_dwordx4 v[126:129], v147, s[16:19], s8 offen
	buffer_load_dwordx4 v[136:139], v148, s[16:19], s8 offen
	buffer_load_dwordx4 v[184:187], v149, s[16:19], s8 offen
	buffer_load_dwordx4 v[204:207], v150, s[16:19], s8 offen
	v_mfma_f32_16x16x32_f16 v[42:45], v[188:191], v[208:211], v[42:45]
	v_mfma_f32_16x16x32_f16 v[46:49], v[188:191], v[212:215], v[46:49]
	v_mfma_f32_16x16x32_f16 v[34:37], v[188:191], v[216:219], v[34:37]
	ds_read_b128 v[188:191], v111 offset:512
	ds_read_b128 v[208:211], v111 offset:16896
	ds_read_b128 v[212:215], v111 offset:33280
	ds_read_b128 v[216:219], v111 offset:49664
	s_add_i32 s8, s22, 0xfffc0000
	s_waitcnt vmcnt(15) lgkmcnt(7)
	v_mfma_f32_16x16x32_f16 v[164:167], v[78:81], v[180:183], v[164:167]
	s_waitcnt lgkmcnt(6)
	v_mfma_f32_16x16x32_f16 v[168:171], v[78:81], v[220:223], v[168:171]
	s_waitcnt lgkmcnt(5)
	v_mfma_f32_16x16x32_f16 v[172:175], v[78:81], v[224:227], v[172:175]
	s_waitcnt lgkmcnt(4)
	v_mfma_f32_16x16x32_f16 v[78:81], v[78:81], v[228:231], v[82:85]
	s_waitcnt vmcnt(14)
	v_mfma_f32_16x16x32_f16 v[58:61], v[122:125], v[180:183], v[58:61]
	v_mfma_f32_16x16x32_f16 v[82:85], v[122:125], v[220:223], v[86:89]
	v_mfma_f32_16x16x32_f16 v[86:89], v[122:125], v[224:227], v[94:97]
	v_mfma_f32_16x16x32_f16 v[70:73], v[122:125], v[228:231], v[70:73]
	s_waitcnt vmcnt(13)
	v_mfma_f32_16x16x32_f16 v[54:57], v[156:159], v[180:183], v[54:57]
	v_mfma_f32_16x16x32_f16 v[74:77], v[156:159], v[220:223], v[74:77]
	v_mfma_f32_16x16x32_f16 v[90:93], v[156:159], v[224:227], v[90:93]
	v_mfma_f32_16x16x32_f16 v[62:65], v[156:159], v[228:231], v[62:65]
	s_waitcnt vmcnt(12)
	v_mfma_f32_16x16x32_f16 v[38:41], v[160:163], v[180:183], v[38:41]
	buffer_load_dwordx4 v[94:97], v147, s[16:19], s8 offen
	buffer_load_dwordx4 v[122:125], v148, s[16:19], s8 offen
	buffer_load_dwordx4 v[156:159], v149, s[16:19], s8 offen
	buffer_load_dwordx4 v[180:183], v150, s[16:19], s8 offen
	v_mfma_f32_16x16x32_f16 v[42:45], v[160:163], v[220:223], v[42:45]
	v_mfma_f32_16x16x32_f16 v[46:49], v[160:163], v[224:227], v[46:49]
	v_mfma_f32_16x16x32_f16 v[34:37], v[160:163], v[228:231], v[34:37]
	ds_read_b128 v[160:163], v98 offset:512
	ds_read_b128 v[220:223], v98 offset:16896
	ds_read_b128 v[224:227], v98 offset:33280
	ds_read_b128 v[228:231], v98 offset:49664
	s_add_i32 s8, s22, 0xfffc8000
	s_waitcnt vmcnt(15) lgkmcnt(7)
	v_mfma_f32_16x16x32_f16 v[164:167], v[66:69], v[188:191], v[164:167]
	s_waitcnt lgkmcnt(6)
	v_mfma_f32_16x16x32_f16 v[168:171], v[66:69], v[208:211], v[168:171]
	s_waitcnt lgkmcnt(5)
	v_mfma_f32_16x16x32_f16 v[172:175], v[66:69], v[212:215], v[172:175]
	s_waitcnt lgkmcnt(4)
	v_mfma_f32_16x16x32_f16 v[66:69], v[66:69], v[216:219], v[78:81]
	s_waitcnt vmcnt(14)
	v_mfma_f32_16x16x32_f16 v[58:61], v[192:195], v[188:191], v[58:61]
	v_mfma_f32_16x16x32_f16 v[78:81], v[192:195], v[208:211], v[82:85]
	v_mfma_f32_16x16x32_f16 v[82:85], v[192:195], v[212:215], v[86:89]
	v_mfma_f32_16x16x32_f16 v[70:73], v[192:195], v[216:219], v[70:73]
	s_waitcnt vmcnt(13)
	v_mfma_f32_16x16x32_f16 v[54:57], v[196:199], v[188:191], v[54:57]
	v_mfma_f32_16x16x32_f16 v[74:77], v[196:199], v[208:211], v[74:77]
	v_mfma_f32_16x16x32_f16 v[86:89], v[196:199], v[212:215], v[90:93]
	v_mfma_f32_16x16x32_f16 v[62:65], v[196:199], v[216:219], v[62:65]
	s_waitcnt vmcnt(12)
	v_mfma_f32_16x16x32_f16 v[38:41], v[200:203], v[188:191], v[38:41]
	buffer_load_dwordx4 v[90:93], v147, s[16:19], s8 offen
	buffer_load_dwordx4 v[188:191], v148, s[16:19], s8 offen
	buffer_load_dwordx4 v[192:195], v149, s[16:19], s8 offen
	buffer_load_dwordx4 v[196:199], v150, s[16:19], s8 offen
	v_mfma_f32_16x16x32_f16 v[42:45], v[200:203], v[208:211], v[42:45]
	v_mfma_f32_16x16x32_f16 v[46:49], v[200:203], v[212:215], v[46:49]
	v_mfma_f32_16x16x32_f16 v[34:37], v[200:203], v[216:219], v[34:37]
	ds_read_b128 v[200:203], v99 offset:512
	ds_read_b128 v[208:211], v99 offset:16896
	ds_read_b128 v[212:215], v99 offset:33280
	ds_read_b128 v[216:219], v99 offset:49664
	s_add_i32 s8, s22, 0xfffd0000
	s_waitcnt vmcnt(15) lgkmcnt(7)
	v_mfma_f32_16x16x32_f16 v[164:167], v[50:53], v[160:163], v[164:167]
	s_waitcnt lgkmcnt(6)
	v_mfma_f32_16x16x32_f16 v[168:171], v[50:53], v[220:223], v[168:171]
	s_waitcnt lgkmcnt(5)
	v_mfma_f32_16x16x32_f16 v[172:175], v[50:53], v[224:227], v[172:175]
	s_waitcnt lgkmcnt(4)
	v_mfma_f32_16x16x32_f16 v[50:53], v[50:53], v[228:231], v[66:69]
	s_waitcnt vmcnt(14)
	v_mfma_f32_16x16x32_f16 v[58:61], v[140:143], v[160:163], v[58:61]
	v_mfma_f32_16x16x32_f16 v[66:69], v[140:143], v[220:223], v[78:81]
	v_mfma_f32_16x16x32_f16 v[78:81], v[140:143], v[224:227], v[82:85]
	v_mfma_f32_16x16x32_f16 v[70:73], v[140:143], v[228:231], v[70:73]
	s_waitcnt vmcnt(13)
	v_mfma_f32_16x16x32_f16 v[54:57], v[152:155], v[160:163], v[54:57]
	v_mfma_f32_16x16x32_f16 v[74:77], v[152:155], v[220:223], v[74:77]
	v_mfma_f32_16x16x32_f16 v[82:85], v[152:155], v[224:227], v[86:89]
	v_mfma_f32_16x16x32_f16 v[62:65], v[152:155], v[228:231], v[62:65]
	s_waitcnt vmcnt(12)
	v_mfma_f32_16x16x32_f16 v[38:41], v[176:179], v[160:163], v[38:41]
	buffer_load_dwordx4 v[86:89], v147, s[16:19], s8 offen
	buffer_load_dwordx4 v[140:143], v148, s[16:19], s8 offen
	buffer_load_dwordx4 v[152:155], v149, s[16:19], s8 offen
	buffer_load_dwordx4 v[160:163], v150, s[16:19], s8 offen
	v_mfma_f32_16x16x32_f16 v[42:45], v[176:179], v[220:223], v[42:45]
	v_mfma_f32_16x16x32_f16 v[46:49], v[176:179], v[224:227], v[46:49]
	v_mfma_f32_16x16x32_f16 v[34:37], v[176:179], v[228:231], v[34:37]
	ds_read_b128 v[176:179], v100 offset:512
	ds_read_b128 v[220:223], v100 offset:16896
	ds_read_b128 v[224:227], v100 offset:33280
	ds_read_b128 v[228:231], v100 offset:49664
	s_add_i32 s8, s22, 0xfffd8000
	s_waitcnt vmcnt(15) lgkmcnt(7)
	v_mfma_f32_16x16x32_f16 v[164:167], v[126:129], v[200:203], v[164:167]
	s_waitcnt lgkmcnt(6)
	v_mfma_f32_16x16x32_f16 v[168:171], v[126:129], v[208:211], v[168:171]
	s_waitcnt lgkmcnt(5)
	v_mfma_f32_16x16x32_f16 v[172:175], v[126:129], v[212:215], v[172:175]
	s_waitcnt lgkmcnt(4)
	v_mfma_f32_16x16x32_f16 v[50:53], v[126:129], v[216:219], v[50:53]
	s_waitcnt vmcnt(14)
	v_mfma_f32_16x16x32_f16 v[58:61], v[136:139], v[200:203], v[58:61]
	v_mfma_f32_16x16x32_f16 v[66:69], v[136:139], v[208:211], v[66:69]
	v_mfma_f32_16x16x32_f16 v[78:81], v[136:139], v[212:215], v[78:81]
	v_mfma_f32_16x16x32_f16 v[70:73], v[136:139], v[216:219], v[70:73]
	s_waitcnt vmcnt(13)
	v_mfma_f32_16x16x32_f16 v[54:57], v[184:187], v[200:203], v[54:57]
	v_mfma_f32_16x16x32_f16 v[74:77], v[184:187], v[208:211], v[74:77]
	v_mfma_f32_16x16x32_f16 v[82:85], v[184:187], v[212:215], v[82:85]
	v_mfma_f32_16x16x32_f16 v[62:65], v[184:187], v[216:219], v[62:65]
	s_waitcnt vmcnt(12)
	v_mfma_f32_16x16x32_f16 v[38:41], v[204:207], v[200:203], v[38:41]
	buffer_load_dwordx4 v[126:129], v147, s[16:19], s8 offen
	buffer_load_dwordx4 v[136:139], v148, s[16:19], s8 offen
	buffer_load_dwordx4 v[184:187], v149, s[16:19], s8 offen
	buffer_load_dwordx4 v[200:203], v150, s[16:19], s8 offen
	v_mfma_f32_16x16x32_f16 v[42:45], v[204:207], v[208:211], v[42:45]
	v_mfma_f32_16x16x32_f16 v[46:49], v[204:207], v[212:215], v[46:49]
	v_mfma_f32_16x16x32_f16 v[34:37], v[204:207], v[216:219], v[34:37]
	ds_read_b128 v[204:207], v111 offset:768
	ds_read_b128 v[208:211], v111 offset:17152
	ds_read_b128 v[212:215], v111 offset:33536
	ds_read_b128 v[216:219], v111 offset:49920
	s_add_i32 s8, s22, 0xfffe0000
	s_waitcnt vmcnt(15) lgkmcnt(7)
	v_mfma_f32_16x16x32_f16 v[164:167], v[94:97], v[176:179], v[164:167]
	s_waitcnt lgkmcnt(6)
	v_mfma_f32_16x16x32_f16 v[168:171], v[94:97], v[220:223], v[168:171]
	s_waitcnt vmcnt(14)
	v_mfma_f32_16x16x32_f16 v[58:61], v[122:125], v[176:179], v[58:61]
	v_mfma_f32_16x16x32_f16 v[66:69], v[122:125], v[220:223], v[66:69]
	s_waitcnt lgkmcnt(5)
	v_mfma_f32_16x16x32_f16 v[78:81], v[122:125], v[224:227], v[78:81]
	s_waitcnt lgkmcnt(4)
	v_mfma_f32_16x16x32_f16 v[70:73], v[122:125], v[228:231], v[70:73]
	s_waitcnt vmcnt(13)
	v_mfma_f32_16x16x32_f16 v[54:57], v[156:159], v[176:179], v[54:57]
	v_mfma_f32_16x16x32_f16 v[74:77], v[156:159], v[220:223], v[74:77]
	v_mfma_f32_16x16x32_f16 v[82:85], v[156:159], v[224:227], v[82:85]
	v_mfma_f32_16x16x32_f16 v[62:65], v[156:159], v[228:231], v[62:65]
	s_waitcnt vmcnt(12)
	v_mfma_f32_16x16x32_f16 v[38:41], v[180:183], v[176:179], v[38:41]
	v_mfma_f32_16x16x32_f16 v[42:45], v[180:183], v[220:223], v[42:45]
	buffer_load_dwordx4 v[122:125], v147, s[16:19], s8 offen
	buffer_load_dwordx4 v[156:159], v148, s[16:19], s8 offen
	buffer_load_dwordx4 v[176:179], v149, s[16:19], s8 offen
	buffer_load_dwordx4 v[220:223], v150, s[16:19], s8 offen
	v_mfma_f32_16x16x32_f16 v[50:53], v[94:97], v[228:231], v[50:53]
	v_mfma_f32_16x16x32_f16 v[46:49], v[180:183], v[224:227], v[46:49]
	v_mfma_f32_16x16x32_f16 v[34:37], v[180:183], v[228:231], v[34:37]
	v_mfma_f32_16x16x32_f16 v[172:175], v[94:97], v[224:227], v[172:175]
	ds_read_b128 v[94:97], v98 offset:768
	ds_read_b128 v[180:183], v98 offset:17152
	ds_read_b128 v[224:227], v98 offset:33536
	ds_read_b128 v[228:231], v98 offset:49920
	s_add_i32 s8, s22, 0xfffe8000
	s_waitcnt vmcnt(15) lgkmcnt(7)
	v_mfma_f32_16x16x32_f16 v[164:167], v[90:93], v[204:207], v[164:167]
	s_waitcnt lgkmcnt(6)
	v_mfma_f32_16x16x32_f16 v[168:171], v[90:93], v[208:211], v[168:171]
	s_waitcnt lgkmcnt(5)
	v_mfma_f32_16x16x32_f16 v[172:175], v[90:93], v[212:215], v[172:175]
	s_waitcnt lgkmcnt(4)
	v_mfma_f32_16x16x32_f16 v[90:93], v[90:93], v[216:219], v[50:53]
	s_waitcnt vmcnt(14)
	v_mfma_f32_16x16x32_f16 v[232:235], v[188:191], v[204:207], v[58:61]
	v_mfma_f32_16x16x32_f16 v[66:69], v[188:191], v[208:211], v[66:69]
	v_mfma_f32_16x16x32_f16 v[78:81], v[188:191], v[212:215], v[78:81]
	v_mfma_f32_16x16x32_f16 v[70:73], v[188:191], v[216:219], v[70:73]
	s_waitcnt vmcnt(13)
	v_mfma_f32_16x16x32_f16 v[188:191], v[192:195], v[204:207], v[54:57]
	v_mfma_f32_16x16x32_f16 v[74:77], v[192:195], v[208:211], v[74:77]
	v_mfma_f32_16x16x32_f16 v[82:85], v[192:195], v[212:215], v[82:85]
	v_mfma_f32_16x16x32_f16 v[62:65], v[192:195], v[216:219], v[62:65]
	s_waitcnt vmcnt(12)
	v_mfma_f32_16x16x32_f16 v[192:195], v[196:199], v[204:207], v[38:41]
	buffer_load_dwordx4 v[58:61], v147, s[16:19], s8 offen
	buffer_load_dwordx4 v[54:57], v148, s[16:19], s8 offen
	buffer_load_dwordx4 v[50:53], v149, s[16:19], s8 offen
	buffer_load_dwordx4 v[38:41], v150, s[16:19], s8 offen
	v_mfma_f32_16x16x32_f16 v[42:45], v[196:199], v[208:211], v[42:45]
	v_mfma_f32_16x16x32_f16 v[46:49], v[196:199], v[212:215], v[46:49]
	v_mfma_f32_16x16x32_f16 v[196:199], v[196:199], v[216:219], v[34:37]
	ds_read_b128 v[204:207], v99 offset:768
	ds_read_b128 v[208:211], v99 offset:17152
	ds_read_b128 v[212:215], v99 offset:33536
	ds_read_b128 v[216:219], v99 offset:49920
	s_add_i32 s8, s22, 0xffff0000
	s_waitcnt vmcnt(15) lgkmcnt(7)
	v_mfma_f32_16x16x32_f16 v[164:167], v[86:89], v[94:97], v[164:167]
	s_waitcnt lgkmcnt(6)
	v_mfma_f32_16x16x32_f16 v[168:171], v[86:89], v[180:183], v[168:171]
	s_waitcnt lgkmcnt(5)
	v_mfma_f32_16x16x32_f16 v[172:175], v[86:89], v[224:227], v[172:175]
	s_waitcnt lgkmcnt(4)
	v_mfma_f32_16x16x32_f16 v[86:89], v[86:89], v[228:231], v[90:93]
	s_waitcnt vmcnt(14)
	v_mfma_f32_16x16x32_f16 v[232:235], v[140:143], v[94:97], v[232:235]
	v_mfma_f32_16x16x32_f16 v[66:69], v[140:143], v[180:183], v[66:69]
	v_mfma_f32_16x16x32_f16 v[236:239], v[140:143], v[224:227], v[78:81]
	v_mfma_f32_16x16x32_f16 v[70:73], v[140:143], v[228:231], v[70:73]
	s_waitcnt vmcnt(13)
	v_mfma_f32_16x16x32_f16 v[140:143], v[152:155], v[94:97], v[188:191]
	v_mfma_f32_16x16x32_f16 v[74:77], v[152:155], v[180:183], v[74:77]
	v_mfma_f32_16x16x32_f16 v[82:85], v[152:155], v[224:227], v[82:85]
	v_mfma_f32_16x16x32_f16 v[62:65], v[152:155], v[228:231], v[62:65]
	s_waitcnt vmcnt(12)
	v_mfma_f32_16x16x32_f16 v[152:155], v[160:163], v[94:97], v[192:195]
	buffer_load_dwordx4 v[94:97], v147, s[16:19], s8 offen
	buffer_load_dwordx4 v[90:93], v148, s[16:19], s8 offen
	buffer_load_dwordx4 v[78:81], v149, s[16:19], s8 offen
	buffer_load_dwordx4 v[34:37], v150, s[16:19], s8 offen
	v_mfma_f32_16x16x32_f16 v[42:45], v[160:163], v[180:183], v[42:45]
	v_mfma_f32_16x16x32_f16 v[46:49], v[160:163], v[224:227], v[46:49]
	v_mfma_f32_16x16x32_f16 v[160:163], v[160:163], v[228:231], v[196:199]
	ds_read_b128 v[180:183], v100 offset:768
	ds_read_b128 v[188:191], v100 offset:17152
	ds_read_b128 v[192:195], v100 offset:33536
	ds_read_b128 v[196:199], v100 offset:49920
	s_add_i32 s8, s22, 0xffff8000
	s_waitcnt vmcnt(15) lgkmcnt(7)
	v_mfma_f32_16x16x32_f16 v[164:167], v[126:129], v[204:207], v[164:167]
	s_waitcnt lgkmcnt(6)
	v_mfma_f32_16x16x32_f16 v[168:171], v[126:129], v[208:211], v[168:171]
	s_waitcnt lgkmcnt(5)
	v_mfma_f32_16x16x32_f16 v[172:175], v[126:129], v[212:215], v[172:175]
	s_waitcnt lgkmcnt(4)
	v_mfma_f32_16x16x32_f16 v[86:89], v[126:129], v[216:219], v[86:89]
	s_waitcnt vmcnt(14)
	v_mfma_f32_16x16x32_f16 v[126:129], v[136:139], v[204:207], v[232:235]
	v_mfma_f32_16x16x32_f16 v[66:69], v[136:139], v[208:211], v[66:69]
	v_mfma_f32_16x16x32_f16 v[224:227], v[136:139], v[212:215], v[236:239]
	v_mfma_f32_16x16x32_f16 v[136:139], v[136:139], v[216:219], v[70:73]
	s_waitcnt vmcnt(13)
	v_mfma_f32_16x16x32_f16 v[140:143], v[184:187], v[204:207], v[140:143]
	v_mfma_f32_16x16x32_f16 v[74:77], v[184:187], v[208:211], v[74:77]
	v_mfma_f32_16x16x32_f16 v[228:231], v[184:187], v[212:215], v[82:85]
	v_mfma_f32_16x16x32_f16 v[184:187], v[184:187], v[216:219], v[62:65]
	s_waitcnt vmcnt(12)
	v_mfma_f32_16x16x32_f16 v[152:155], v[200:203], v[204:207], v[152:155]
	v_mfma_f32_16x16x32_f16 v[204:207], v[200:203], v[208:211], v[42:45]
	buffer_load_dwordx4 v[82:85], v147, s[16:19], s8 offen
	buffer_load_dwordx4 v[70:73], v148, s[16:19], s8 offen
	buffer_load_dwordx4 v[62:65], v149, s[16:19], s8 offen
	buffer_load_dwordx4 v[42:45], v150, s[16:19], s8 offen
	v_mfma_f32_16x16x32_f16 v[46:49], v[200:203], v[212:215], v[46:49]
	v_mfma_f32_16x16x32_f16 v[160:163], v[200:203], v[216:219], v[160:163]
	v_add_u32_e32 v0, 0x1ac00, v104
	ds_read_b128 v[240:243], v0
	ds_read_b128 v[244:247], v0 offset:16
	s_waitcnt vmcnt(12) lgkmcnt(5)
	v_mfma_f32_16x16x32_f16 v[164:167], v[122:125], v[180:183], v[164:167]
	v_mfma_f32_16x16x32_f16 v[126:129], v[156:159], v[180:183], v[126:129]
	v_mfma_f32_16x16x32_f16 v[140:143], v[176:179], v[180:183], v[140:143]
	v_mfma_f32_16x16x32_f16 v[152:155], v[220:223], v[180:183], v[152:155]
	s_waitcnt lgkmcnt(4)
	v_mfma_f32_16x16x32_f16 v[168:171], v[122:125], v[188:191], v[168:171]
	v_mfma_f32_16x16x32_f16 v[208:211], v[156:159], v[188:191], v[66:69]
	v_mfma_f32_16x16x32_f16 v[212:215], v[176:179], v[188:191], v[74:77]
	v_mfma_f32_16x16x32_f16 v[204:207], v[220:223], v[188:191], v[204:207]
	s_waitcnt lgkmcnt(3)
	v_mfma_f32_16x16x32_f16 v[172:175], v[122:125], v[192:195], v[172:175]
	v_cvt_pk_f16_f32 v232, v164, v165
	v_cvt_pk_f16_f32 v233, v166, v167
	v_pk_max_f16 v232, v232, 0
	v_pk_max_f16 v233, v233, 0
	v_mfma_f32_16x16x32_f16 v[224:227], v[156:159], v[192:195], v[224:227]
	v_cvt_pk_f16_f32 v234, v126, v127
	v_cvt_pk_f16_f32 v235, v128, v129
	v_pk_max_f16 v234, v234, 0
	v_pk_max_f16 v235, v235, 0
	v_mfma_f32_16x16x32_f16 v[228:231], v[176:179], v[192:195], v[228:231]
	v_cvt_pk_f16_f32 v236, v140, v141
	v_cvt_pk_f16_f32 v237, v142, v143
	v_pk_max_f16 v236, v236, 0
	v_pk_max_f16 v237, v237, 0
	v_mfma_f32_16x16x32_f16 v[216:219], v[220:223], v[192:195], v[46:49]
	v_cvt_pk_f16_f32 v238, v152, v153
	v_cvt_pk_f16_f32 v239, v154, v155
	v_pk_max_f16 v238, v238, 0
	v_pk_max_f16 v239, v239, 0
	s_waitcnt lgkmcnt(2)
	v_mfma_f32_16x16x32_f16 v[200:203], v[122:125], v[196:199], v[86:89]
	v_cvt_pk_f16_f32 v180, v168, v169
	v_cvt_pk_f16_f32 v181, v170, v171
	v_pk_max_f16 v180, v180, 0
	v_pk_max_f16 v181, v181, 0
	buffer_load_dwordx4 v[86:89], v147, s[16:19], s22 offen
	buffer_load_dwordx4 v[74:77], v148, s[16:19], s22 offen
	buffer_load_dwordx4 v[66:69], v149, s[16:19], s22 offen
	buffer_load_dwordx4 v[46:49], v150, s[16:19], s22 offen
	v_mfma_f32_16x16x32_f16 v[136:139], v[156:159], v[196:199], v[136:139]
	v_cvt_pk_f16_f32 v182, v208, v209
	v_cvt_pk_f16_f32 v183, v210, v211
	v_pk_max_f16 v182, v182, 0
	v_pk_max_f16 v183, v183, 0
	s_waitcnt lgkmcnt(1)
	v_mfma_f32_16x16x32_f16 v[252:255], v[240:243], v[232:235], 0
	v_cvt_pk_f16_f32 v232, v172, v173
	v_cvt_pk_f16_f32 v233, v174, v175
	v_pk_max_f16 v232, v232, 0
	v_pk_max_f16 v233, v233, 0
	v_mfma_f32_16x16x32_f16 v[184:187], v[176:179], v[196:199], v[184:187]
	v_cvt_pk_f16_f32 v188, v212, v213
	v_cvt_pk_f16_f32 v189, v214, v215
	v_pk_max_f16 v188, v188, 0
	v_pk_max_f16 v189, v189, 0
	s_waitcnt lgkmcnt(0)
	v_mfma_f32_16x16x32_f16 v[252:255], v[244:247], v[236:239], v[252:255]
	v_cvt_pk_f16_f32 v234, v224, v225
	v_cvt_pk_f16_f32 v235, v226, v227
	v_pk_max_f16 v234, v234, 0
	v_pk_max_f16 v235, v235, 0
	v_mfma_f32_16x16x32_f16 v[160:163], v[220:223], v[196:199], v[160:163]
	v_cvt_pk_f16_f32 v190, v204, v205
	v_cvt_pk_f16_f32 v191, v206, v207
	v_pk_max_f16 v190, v190, 0
	v_pk_max_f16 v191, v191, 0
	v_mfma_f32_16x16x32_f16 v[192:195], v[240:243], v[180:183], 0
	v_cvt_pk_f16_f32 v236, v228, v229
	v_cvt_pk_f16_f32 v237, v230, v231
	v_pk_max_f16 v236, v236, 0
	v_pk_max_f16 v237, v237, 0
	v_mfma_f32_16x16x32_f16 v[192:195], v[244:247], v[188:191], v[192:195]
	v_cvt_pk_f16_f32 v238, v216, v217
	v_cvt_pk_f16_f32 v239, v218, v219
	v_pk_max_f16 v238, v238, 0
	v_pk_max_f16 v239, v239, 0
	v_cvt_pk_f16_f32 v180, v200, v201
	v_cvt_pk_f16_f32 v181, v202, v203
	v_pk_max_f16 v180, v180, 0
	v_pk_max_f16 v181, v181, 0
	v_mfma_f32_16x16x32_f16 v[196:199], v[240:243], v[232:235], 0
	v_cvt_pk_f16_f32 v182, v136, v137
	v_cvt_pk_f16_f32 v183, v138, v139
	v_pk_max_f16 v182, v182, 0
	v_pk_max_f16 v183, v183, 0
	v_mfma_f32_16x16x32_f16 v[196:199], v[244:247], v[236:239], v[196:199]
	v_cvt_pk_f16_f32 v188, v184, v185
	v_cvt_pk_f16_f32 v189, v186, v187
	v_pk_max_f16 v188, v188, 0
	v_pk_max_f16 v189, v189, 0
	v_cvt_pk_f16_f32 v190, v160, v161
	v_cvt_pk_f16_f32 v191, v162, v163
	v_pk_max_f16 v190, v190, 0
	v_pk_max_f16 v191, v191, 0
	v_mfma_f32_16x16x32_f16 v[122:125], v[240:243], v[180:183], 0
	s_nop 0
	v_mfma_f32_16x16x32_f16 v[122:125], v[244:247], v[188:191], v[122:125]
	v_add_u32_e32 v145, 0x12c00, v105
	ds_read_b128 v[240:243], v145 offset:2048
	ds_read_b128 v[244:247], v145 offset:2064
	ds_read_b128 v[248:251], v145 offset:2080
	s_load_dword s30, s[12:13], 0x0
	v_cndmask_b32_e64 v0, v252, v192, s[2:3]
	ds_read_b128 v[252:255], v145 offset:2096
	ds_read_u16 v102, v114
	ds_read_u16 v103, v114 offset:512
	ds_read_u16 v115, v114 offset:1024
	ds_read_u16 v116, v114 offset:1536
	v_cndmask_b32_e64 v0, v0, v196, s[0:1]
	s_waitcnt vmcnt(16)
	v_cndmask_b32_e64 v1, v30, v134, s[0:1]
	v_bfi_b32 v30, s10, v1, v30
	v_perm_b32 v1, v22, v134, s24
	v_cndmask_b32_e64 v22, v22, v1, s[0:1]
	v_bfi_b32 v1, s10, v135, v18
	v_perm_b32 v121, v10, v135, s24
	v_cndmask_b32_e64 v18, v18, v1, s[0:1]
	v_cndmask_b32_e64 v10, v10, v121, s[0:1]
	v_cndmask_b32_e64 v0, v0, v122, s[26:27]
	ds_write_b32 v112, v0
	s_waitcnt lgkmcnt(0)
	s_barrier
	ds_read_b128 v[232:235], v113
	ds_read_b128 v[236:239], v113 offset:1024
	s_waitcnt lgkmcnt(0)
	v_add_f32_e32 v0, v232, v233
	v_add_f32_e32 v1, v234, v235
	v_add_f32_e32 v121, v236, v237
	v_add_f32_e32 v144, v238, v239
	v_add_f32_e32 v0, v0, v1
	v_add_f32_e32 v121, v121, v144
	v_add_f32_e32 v0, v0, v121
	v_add_f32_e32 v0, s30, v0
	ds_write_b32 v106, v0
	v_cvt_f16_f32_e32 v1, v0
	v_cvt_f16_f32_e32 v121, v0
	s_nop 1
	v_permlane16_swap_b32_e32 v1, v121
	v_mov_b32_e32 v144, v1
	v_mov_b32_e32 v145, v121
	s_nop 1
	v_permlane32_swap_b32_e32 v1, v144
	v_permlane32_swap_b32_e32 v121, v145
	s_branch .LBB1_3
